# v72 with 256 conversion items shifted from the upper to the lower grid half in layer 0's in-projection tail (5064/696): the upper half also carries the cumulative-sum units
# baseline (speedup 1.0000x reference)
; #define LAS __attribute__((address_space(3)))
; __device__ __forceinline__ int opaque_tid() { int t = threadIdx.x; asm volatile("" : "+v"(t)); return t; }
;     __device__ __forceinline__ bool next(int i, Unit& u) const {
;         const long L = (long)i * G + c; if (L >= nwg) return false;
;         int wgid = (int)L; { const int q = nwg / NXCD, r = nwg % NXCD, xcd = wgid % NXCD, off = wgid / NXCD; wgid = (xcd < r ? xcd * (q + 1) : r * (q + 1) + (xcd - r) * q) + off; }
;         const int nig = WGM * nN, gid = wgid / nig, fm = gid * WGM, gsz = (nM - fm) < WGM ? (nM - fm) : WGM;
;         u.pm = fm + ((wgid % nig) % gsz); u.pn = (wgid % nig) / gsz; u.e = 0; u.rows = 256;
;         u.a = A + (size_t)u.pm * tstepA; u.b = Bt + (size_t)u.pn * tstep; return true;
; __device__ __forceinline__ void pj_mfma(const Args& a, LAS unsigned char* lds, int layer) {
;     pg8::DenseOrder So; So.init(a.ws + WS_ACT, a.ws + WS_WIN + (size_t)layer * 3328 * D * 2, NTOK, 3328, D, gridDim.x, blockIdx.x);
;     LAS float* gl = (LAS float*)(lds + SEG_OFF + 256);
;     { const int t_ = opaque_tid(); if (t_ < 256) { const int w = t_ >> 6, i = t_ & 63; const float* gp_ = w == 0 ? a.in[I_QGF] : w == 1 ? a.in[I_KGF] : w == 2 ? a.in[I_QGD] : a.in[I_KGD]; gl[t_] = gp_[layer * 64 + i]; } }
;     __syncthreads();
;     EpiProj E{(bf16_t*)(a.ws + WS_PROJ), gl};
;     pg8::gemm_phase<EpiProj, pg8::DenseOrder>(lds, D, So, E);
;     if ((int)blockIdx.x >= (int)gridDim.x - 32) cumsum_unit(a, lds, blockIdx.x - (gridDim.x - 32));
;     if (layer + 1 < NL) { __syncthreads(); constexpr int I_SPLIT = 10240;
;         const int half = gridDim.x / 2; const bool upper = (int)blockIdx.x >= half;
;         p0_prep(a, lds, layer + 1, upper ? half : 0, upper ? (int)gridDim.x - half : half, upper ? 0 : I_SPLIT, upper ? I_SPLIT : (1 << 30)); }
.LBB0_101:
	s_or_b64 exec, exec, s[0:1]
	s_mov_b32 vcc_lo, 0
	s_nop 1
	v_writelane_b32 v254, vcc_lo, 60
	s_nop 1
	s_mov_b32 vcc_lo, 0
	s_nop 1
	v_writelane_b32 v254, vcc_lo, 62
	s_nop 1
	s_waitcnt lgkmcnt(0)
	s_barrier
	s_load_dwordx2 s[92:93], s[54:55], 0xa0
	s_load_dwordx16 s[12:27], s[54:55], 0x20
	s_load_dwordx4 s[0:3], s[54:55], 0x90
	s_movk_i32 s5, 0xd1
	s_mov_b32 s67, 0
	s_waitcnt vmcnt(0)
	v_mbcnt_lo_u32_b32 v1, -1, 0
	v_mbcnt_hi_u32_b32 v199, -1, v1
	s_waitcnt lgkmcnt(0)
	v_writelane_b32 v252, s0, 8
	v_and_b32_e32 v240, 64, v199
	s_mul_hi_u32 s85, s77, 0x600
	v_writelane_b32 v252, s1, 9
	v_writelane_b32 v252, s2, 10
	v_writelane_b32 v252, s3, 11
	s_add_u32 s0, s92, 0x100000
	s_addc_u32 s1, s93, 0
	v_writelane_b32 v252, s0, 12
	s_add_u32 s96, s92, 0xbc00000
	s_addc_u32 s97, s93, 0
	v_writelane_b32 v252, s1, 13
	s_lshl_b32 s0, s61, 3
	s_add_u32 s10, s92, 0x180000
	s_addc_u32 s11, s93, 0
	s_add_u32 s80, s92, 0x7c00000
	s_addc_u32 s81, s93, 0
	v_writelane_b32 v252, s0, 14
	s_add_u32 s0, s92, 0xfc00000
	s_addc_u32 s1, s93, 0
	s_add_u32 s50, s92, 0x18c00000
	s_addc_u32 s51, s93, 0
	s_add_u32 s2, s92, 0xa00000
	s_addc_u32 s3, s93, 0
	v_writelane_b32 v252, s2, 15
	s_cmpk_lt_i32 s61, 0x680
	s_mul_i32 s84, s77, 0x600
	v_writelane_b32 v252, s3, 16
	s_cselect_b64 s[2:3], -1, 0
	v_writelane_b32 v252, s2, 17
	v_mov_b32_e32 v35, 0
	v_add_u32_e32 v241, 64, v240
	v_writelane_b32 v252, s3, 18
	s_ashr_i32 s2, s61, 31
	v_writelane_b32 v252, s2, 19
	s_lshr_b32 s2, s2, 29
	s_add_i32 s3, s61, s2
	s_ashr_i32 s2, s3, 3
	s_and_b32 s3, s3, -8
	s_sub_i32 s3, s61, s3
	s_lshl_b32 s4, s3, 6
	s_cmp_lt_i32 s3, 0
	s_cselect_b32 s5, s5, 0xd0
	s_mul_i32 s5, s5, s3
	s_mulk_i32 s3, 0x41
	s_cselect_b32 s3, s3, s4
	s_add_i32 s5, s5, s2
	s_mul_hi_i32 s4, s5, 0x4ec4ec4f
	s_lshr_b32 s6, s4, 31
	s_ashr_i32 s4, s4, 5
	s_add_i32 s4, s4, s6
	s_mul_i32 s6, s4, 0x68
	s_sub_i32 s5, s5, s6
	s_lshl_b32 s7, s4, 3
	s_bfe_i32 s4, s5, 0x80000
	s_bfe_u32 s4, s4, 0x3000c
	s_add_i32 s6, s5, s4
	s_bfe_i32 s4, s6, 0x80000
	s_and_b32 s6, s6, 0xf8
	s_sub_i32 s5, s5, s6
	s_sext_i32_i16 s8, s4
	s_sext_i32_i8 s5, s5
	s_add_i32 s28, s7, s5
	s_ashr_i32 s5, s8, 3
	v_writelane_b32 v252, s5, 20
	s_mov_b32 s6, s28
	s_ashr_i32 s29, s28, 31
	v_writelane_b32 v252, s6, 21
	s_lshr_b32 s4, s8, 3
	v_xor_b32_e32 v236, 16, v199
	v_writelane_b32 v252, s7, 22
	s_lshl_b64 s[6:7], s[28:29], 19
	s_add_u32 s6, s80, s6
	s_addc_u32 s7, s81, s7
	v_writelane_b32 v252, s6, 23
	s_bfe_i64 s[4:5], s[4:5], 0x100000
	s_lshl_b64 s[4:5], s[4:5], 19
	v_writelane_b32 v252, s7, 24
	v_writelane_b32 v252, s4, 25
	v_xor_b32_e32 v237, 32, v199
	v_mov_b32_e32 v238, 1
	v_writelane_b32 v252, s5, 26
	s_ashr_i32 s4, s77, 31
	v_writelane_b32 v252, s4, 27
	s_sub_i32 s4, s77, 32
	s_cmp_ge_i32 s61, s4
	s_cselect_b64 s[6:7], -1, 0
	v_writelane_b32 v252, s6, 28
	s_sub_i32 s4, s61, s4
	s_and_b32 s5, s4, 3
	v_writelane_b32 v252, s7, 29
	s_ashr_i32 s6, s4, 2
	s_ashr_i32 s7, s6, 31
	s_lshl_b32 s5, s5, 2
	s_add_u32 s5, s10, s5
	v_writelane_b32 v252, s10, 30
	s_addc_u32 s8, s11, 0
	s_lshl_b64 s[6:7], s[6:7], 16
	s_add_u32 s6, s5, s6
	s_addc_u32 s7, s8, s7
	s_add_u32 s28, s92, 0x200000
	s_addc_u32 s29, s93, 0
	s_ashr_i32 s5, s4, 31
	s_lshl_b64 s[4:5], s[4:5], 14
	v_writelane_b32 v252, s11, 31
	s_add_u32 s4, s28, s4
	v_writelane_b32 v252, s6, 32
	s_addc_u32 s5, s29, s5
	s_lshr_b32 s8, s77, 1
	v_writelane_b32 v252, s7, 33
	s_sub_i32 s9, s77, s8
	v_writelane_b32 v252, s4, 34
	s_cmp_lt_i32 s61, s8
	v_mov_b32_e32 v198, 0x358637bd
	v_writelane_b32 v252, s5, 35
	s_cselect_b64 s[4:5], -1, 0
	s_and_b64 s[6:7], s[4:5], exec
	s_cselect_b32 s6, s8, s9
	s_movk_i32 s7, 0x1680
	s_cselect_b32 s10, 0, s8
	s_cselect_b32 s8, 0x13c8, 0
	s_cselect_b32 s7, s7, 0x13c8
	s_lshl_b32 s6, s6, 3
	v_writelane_b32 v252, s7, 36
	s_cmp_ge_i32 s61, s10
	v_writelane_b32 v252, s6, 37
	s_cselect_b64 s[6:7], -1, 0
	s_or_b64 s[4:5], s[36:37], s[4:5]
	s_load_dwordx8 s[36:43], s[54:55], 0x60
	s_and_b64 s[4:5], s[6:7], s[4:5]
	v_writelane_b32 v252, s4, 38
	v_mov_b32_e32 v201, 1.0
	v_mov_b32_e32 v239, 0x7f800000
	v_writelane_b32 v252, s5, 39
	s_sub_i32 s4, s61, s10
	s_lshl_b32 s4, s4, 3
	s_add_i32 s4, s4, s8
	s_waitcnt lgkmcnt(0)
	s_mov_b64 s[8:9], s[40:41]
	v_writelane_b32 v252, s4, 40
	s_add_u32 s6, s38, 0x400000
	s_mov_b64 s[10:11], s[42:43]
	s_mov_b64 s[4:5], s[36:37]
	v_writelane_b32 v252, s4, 41
	v_mov_b32_e32 v202, 0x3f317218
	v_mov_b32_e32 v242, 0xff800000
	v_writelane_b32 v252, s5, 42
	v_writelane_b32 v252, s6, 43
	v_writelane_b32 v252, s7, 44
	v_writelane_b32 v252, s8, 45
	v_writelane_b32 v252, s9, 46
	v_writelane_b32 v252, s10, 47
	v_writelane_b32 v252, s11, 48
	s_addc_u32 s7, s39, 0
	v_writelane_b32 v252, s6, 49
	s_add_u32 s4, s16, 0xd04000
	s_movk_i32 s74, 0x1ff
	v_writelane_b32 v252, s7, 50
	v_writelane_b32 v252, s12, 51
	s_addc_u32 s5, s17, 0
	s_mov_b32 s76, 0x800000
	v_writelane_b32 v255, s25, 0
	v_writelane_b32 v255, s26, 1
	v_writelane_b32 v255, s27, 2
	v_writelane_b32 v255, s4, 3
	v_writelane_b32 v252, s13, 52
	v_writelane_b32 v252, s14, 53
	v_writelane_b32 v255, s5, 4
	s_add_u32 s4, s92, 0x5b00000
	s_addc_u32 s5, s93, 0
	v_writelane_b32 v255, s4, 5
	v_writelane_b32 v252, s15, 54
	v_writelane_b32 v252, s16, 55
	v_writelane_b32 v255, s5, 6
	s_add_u32 s4, s92, 0x1b00000
	s_addc_u32 s5, s93, 0
	s_add_u32 s82, s92, 0x700000
	v_writelane_b32 v255, s4, 7
	s_addc_u32 s83, s93, 0
	v_writelane_b32 v252, s17, 56
	v_writelane_b32 v255, s5, 8
	s_add_u32 s4, s92, 0x14000
	v_writelane_b32 v255, s4, 9
	s_addc_u32 s4, s93, 0
	s_add_i32 s6, s61, 0x900
	s_cmpk_lt_i32 s61, 0x200
	v_writelane_b32 v255, s4, 10
	s_cselect_b64 s[4:5], -1, 0
	v_writelane_b32 v255, s4, 11
	v_writelane_b32 v252, s18, 57
;     ...
;         if (u < AT_NFOX) {
;             const int qb = 15 - (u >> 5), bh = u & 31, b = bh >> 2, h = bh & 3, q0 = qb * 256;
;             const size_t rb = (size_t)b * S;
;             const bf16_t* Kb = proj + ((size_t)(4 + h) * NTOK + rb) * 64;
;             const bf16_t* Vb = proj + ((size_t)(8 + h) * NTOK + rb) * 64;
;             const float* cum = cumall + (size_t)bh * S;
;             const int jhi = 4 * qb + 3;
;             fox_cr = cum[q0]; fox_cv = cum[64 * (lane <= jhi ? lane : jhi) + 63]; fox_cq = cum[q0 + 32 * wid + r32];
;             if (!(dbg & 1)) { FOX_ISSUE(0); FOX_ISSUE(1); FOX_ISSUE(2); }
;             const bf16_t* Q = proj + ((size_t)(0 + h) * NTOK + rb + q0 + 32 * wid + r32) * 64;
; #pragma unroll
;             for (int d0 = 0; d0 < 4; ++d0) qr[d0] = *(const bf16x8*)(Q + d0 * 16 + hi * 8);
;         } else if (u < AT_NFOX + AT_NDIL) {
;             const int v2 = u - AT_NFOX, bh = v2 % 48, rest = v2 / 48, b = bh / 6, h = bh % 6, p = rest >> 4, x = rest & 15;
;             const int dil = p == 0 ? 1 : p == 1 ? 4 : 16, res = x % dil, nb2 = x / dil;
;             const size_t rb = (size_t)b * S;
;             const bf16_t* Kb = proj + ((size_t)(22 + h) * NTOK + rb) * 64;
;             const bf16_t* Vb = proj + ((size_t)(28 + h) * NTOK + rb) * 64;
;             const int mk_base = 256 * nb2 - 128, tt_lo = nb2 == 0 ? 2 : 0;
;             const size_t rs = (size_t)64 * dil;
; #pragma unroll
;     ...
;             if (tid < 256) { const int st = tid - 64; tab[tid] = (st >= 0 && st <= 128) ? relb[t5_bucket(st * dil) * 6 + h] : -INFINITY; }
;             const size_t trow = (size_t)(256 * nb2 + 32 * wid + r32) * dil + res;
;             const bf16_t* Q = proj + ((size_t)(16 + h) * NTOK + rb + trow) * 64;
; #pragma unroll
;             for (int d0 = 0; d0 < 4; ++d0) qr[d0] = *(const bf16x8*)(Q + d0 * 16 + hi * 8);
;         } else {
;             const int v2 = u - AT_NFOX - AT_NDIL, qb = 15 - v2 / 48, bh = v2 % 48, b = bh / 6, h = bh % 6, q0 = qb * 256;
;             const size_t rb = (size_t)b * S;
;             const bf16_t* Kb = proj + ((size_t)(40 + h) * NTOK + rb) * 64;
;             const bf16_t* Vb = proj + ((size_t)(46 + h) * NTOK + rb) * 64;
;             const int jhi = (q0 + 254) >> 6;
;             if (!(dbg & 1)) { SB_ISSUE(0); SB_ISSUE(1); SB_ISSUE(2); }
	v_writelane_b32 v252, s19, 58
	v_writelane_b32 v255, s5, 12
	s_and_b64 s[4:5], s[4:5], exec
	s_cselect_b32 s13, s61, s6
	s_cmpk_lt_i32 s13, 0xe00
	s_cselect_b64 s[4:5], -1, 0
	v_writelane_b32 v255, s4, 13
	s_cmpk_gt_i32 s13, 0x1ff
	s_mov_b32 s17, s67
	v_writelane_b32 v255, s5, 14
	s_cselect_b64 s[4:5], -1, 0
	v_writelane_b32 v255, s4, 15
	s_cmpk_gt_u32 s13, 0xaff
	v_writelane_b32 v252, s20, 59
	v_writelane_b32 v255, s5, 16
	s_cselect_b64 s[4:5], -1, 0
	v_writelane_b32 v255, s4, 17
	v_writelane_b32 v252, s21, 60
	s_mov_b32 s21, s67
	v_writelane_b32 v255, s5, 18
	s_add_i32 s4, s13, 0xf500
	s_and_b32 s5, s4, 0xffff
	s_mul_i32 s5, s5, 0xaaab
	s_lshr_b32 s5, s5, 21
	s_mul_i32 s6, s5, 48
	s_sub_i32 s4, s4, s6
	s_and_b32 s6, s4, 0xff
	s_mulk_i32 s6, 0xab
	s_bfe_u32 s6, s6, 0x6000a
	s_mul_i32 s7, s6, 6
	s_sub_i32 s4, s4, s7
	s_and_b32 s4, s4, 0xff
	s_lshl_b32 s6, s6, 12
	s_lshl_b32 s4, s4, 15
	s_add_i32 s7, s6, s4
	s_lshl_b32 s7, s7, 7
	s_add_i32 s8, s7, 0xb800000
	s_add_u32 s8, s96, s8
	s_addc_u32 s9, s97, 0
	s_add_i32 s7, s7, 0xa000000
	s_add_u32 s7, s96, s7
	s_addc_u32 s10, s97, 0
	s_lshl_b32 s11, s5, 14
	s_sub_i32 s12, 0x3f000, s11
	s_lshl_b32 s12, s12, 1
	s_add_u32 s14, s7, s12
	s_addc_u32 s15, s10, 0
	v_writelane_b32 v255, s14, 19
	v_writelane_b32 v252, s22, 61
	v_writelane_b32 v252, s23, 62
	v_writelane_b32 v255, s15, 20
	s_add_u32 s14, s8, s12
	s_addc_u32 s15, s9, 0
	s_sub_i32 s12, 0x3e000, s11
	v_writelane_b32 v255, s14, 21
	s_lshl_b32 s12, s12, 1
	v_writelane_b32 v252, s24, 63
	v_writelane_b32 v255, s15, 22
	s_add_u32 s14, s7, s12
	s_addc_u32 s15, s10, 0
	v_writelane_b32 v255, s14, 23
	s_movk_i32 s56, 0x7f
	s_mov_b32 s57, 0xff800000
	v_writelane_b32 v255, s15, 24
	s_add_u32 s14, s8, s12
	s_addc_u32 s15, s9, 0
	s_sub_i32 s11, 0x3d000, s11
	v_writelane_b32 v255, s14, 25
	s_lshl_b32 s11, s11, 1
	s_mov_b32 s65, 0xc2ce8ed0
	v_writelane_b32 v255, s15, 26
	s_add_u32 s14, s7, s11
	s_addc_u32 s15, s10, 0
	s_add_u32 s8, s8, s11
	s_addc_u32 s9, s9, 0
	s_lshl_b32 s5, s5, 8
	s_sub_i32 s4, s4, s5
	s_add_i32 s5, s13, 0xfe00
	s_add_i32 s4, s4, s6
	s_and_b32 s6, s5, 0xffff
	s_mul_i32 s6, s6, 0xaaab
	s_lshr_b32 s7, s6, 21
	s_mul_i32 s7, s7, 48
	s_sub_i32 s5, s5, s7
	v_writelane_b32 v255, s14, 27
	s_and_b32 s7, s5, 0xff
	s_mulk_i32 s7, 0xab
	v_writelane_b32 v255, s15, 28
	v_writelane_b32 v255, s8, 29
	s_bfe_u32 s7, s7, 0x6000a
	s_add_i32 s4, s4, 0x110f00
	v_writelane_b32 v255, s9, 30
	s_mul_i32 s8, s7, 6
	s_sub_i32 s5, s5, s8
	s_and_b32 s5, s5, 0xff
	s_lshl_b32 s7, s7, 12
	s_lshl_b32 s8, s5, 15
	s_add_i32 s7, s7, s8
	v_writelane_b32 v255, s4, 31
	s_bfe_u32 s4, s6, 0x40015
	s_lshl_b32 s6, s7, 7
	s_add_u32 s6, s96, s6
	s_addc_u32 s8, s97, 0
	s_add_u32 s9, s6, 0x5800000
	s_addc_u32 s10, s8, 0
	s_add_u32 s6, s6, 0x7000000
	s_addc_u32 s8, s8, 0
	s_lshl_b32 s11, s4, 7
	s_or_b32 s12, s11, 0x60000
	s_add_u32 s14, s9, s12
	s_addc_u32 s15, s10, 0
	v_writelane_b32 v255, s14, 32
	s_mov_b64 s[44:45], -1
	s_mov_b64 s[86:87], 0x800
	v_writelane_b32 v255, s15, 33
	s_add_u32 s14, s6, s12
	s_addc_u32 s15, s8, 0
	v_writelane_b32 v255, s14, 34
	s_or_b32 s12, s11, 0x40000
	s_mov_b32 s60, 0xbfb8aa3b
	v_writelane_b32 v255, s15, 35
	s_add_u32 s14, s9, s12
	s_addc_u32 s15, s10, 0
	v_writelane_b32 v255, s14, 36
	s_mov_b64 s[88:89], 0x80
	s_mov_b64 s[94:95], 0x100
	v_writelane_b32 v255, s15, 37
	s_add_u32 s14, s6, s12
	s_addc_u32 s15, s8, 0
	v_writelane_b32 v255, s14, 38
	s_or_b32 s12, s11, 0x20000
	s_mov_b32 s62, s67
	v_writelane_b32 v255, s15, 39
	s_add_u32 s14, s9, s12
	s_addc_u32 s15, s10, 0
	v_writelane_b32 v255, s14, 40
	s_nop 1
	v_writelane_b32 v255, s15, 41
	s_add_u32 s14, s6, s12
	s_addc_u32 s15, s8, 0
	v_writelane_b32 v255, s14, 42
	s_nop 1
	v_writelane_b32 v255, s15, 43
	s_add_u32 s14, s9, s11
	s_addc_u32 s15, s10, 0
	v_writelane_b32 v255, s14, 44
	s_add_u32 s10, s6, s11
	s_addc_u32 s11, s8, 0
	v_writelane_b32 v255, s15, 45
	s_lshl_b32 s5, s5, 2
	v_writelane_b32 v255, s10, 46
	s_add_i32 s5, s5, 0
	s_add_i32 s5, s5, 0x21f00
	v_writelane_b32 v255, s11, 47
	v_writelane_b32 v255, s5, 48
	s_ashr_i32 s5, s13, 5
	s_or_b32 s4, s7, s4
	s_sub_i32 s5, 15, s5
	s_lshl_b32 s6, s13, 10
	s_and_b32 s7, s13, 31
	s_and_b32 s6, s6, 0x7000
	s_lshl_b32 s7, s7, 14
	s_or_b32 s14, s4, 0x80000
	s_and_b32 s8, s13, 3
	s_lshl_b32 s16, s5, 8
	s_add_u32 s18, s28, s7
	s_addc_u32 s19, s29, 0
	s_lshl_b32 s7, s5, 2
	v_writelane_b32 v255, s13, 49
	s_or_b32 s20, s7, 3
	s_lshl_b64 s[4:5], s[16:17], 2
	v_writelane_b32 v255, s28, 50
	s_add_u32 s4, s18, s4
	v_writelane_b32 v255, s29, 51
	s_addc_u32 s5, s19, s5
	v_writelane_b32 v255, s4, 52
	s_mov_b32 s15, s67
	s_nop 0
	v_writelane_b32 v255, s5, 53
	s_lshl_b32 s4, s8, 22
	s_lshl_b32 s5, s6, 7
	s_or_b32 s4, s5, s4
	s_add_u32 s4, s96, s4
	s_addc_u32 s5, s97, 0
	s_add_u32 s9, s4, 0x2000000
	s_addc_u32 s10, s5, 0
	s_add_u32 s11, s4, 0x1000000
	s_addc_u32 s12, s5, 0
	s_lshl_b64 s[4:5], s[20:21], 13
	s_add_u32 s22, s11, s4
	s_addc_u32 s23, s12, s5
	v_writelane_b32 v255, s22, 54
	s_add_u32 s4, s9, s4
	s_addc_u32 s5, s10, s5
	v_writelane_b32 v255, s23, 55
	v_writelane_b32 v255, s4, 56
	s_lshl_b32 s66, s20, 6
	s_nop 0
	v_writelane_b32 v255, s5, 57
	s_mov_b32 s4, s20
	v_writelane_b32 v255, s4, 58
	s_nop 1
	v_writelane_b32 v255, s5, 59
	s_lshl_b64 s[4:5], s[66:67], 2
	s_add_u32 s4, s18, s4
	s_addc_u32 s5, s19, s5
; #define LAS __attribute__((address_space(3)))
; #define FOX_ISSUE(i) do { const int j_ = jhi - (i), bf_ = (i) & 3; dma_kv(lds, bf_, Kb + (size_t)j_ * 4096, Vb + (size_t)j_ * 4096, 64, wid, lane); \
;         glds4(cum + j_ * 64 + lane, (unsigned)__builtin_amdgcn_readfirstlane(l0 + L_CK + bf_ * 256)); } while (0)
;     ...
;     bf16x8 qr[4];
;     float fox_cr = 0.f, fox_cv = 0.f, fox_cq = 0.f;
;     auto prologue = [&](int u) {
;         if (!UNIT_ON(u)) return;
;         int lane = tid & 63; asm volatile("" : "+v"(lane));
;         const int r32 = lane & 31, hi = lane >> 5;
;         if (u < AT_NFOX) {
;             const int qb = 15 - (u >> 5), bh = u & 31, b = bh >> 2, h = bh & 3, q0 = qb * 256;
;             const size_t rb = (size_t)b * S;
;             const bf16_t* Kb = proj + ((size_t)(4 + h) * NTOK + rb) * 64;
;             const bf16_t* Vb = proj + ((size_t)(8 + h) * NTOK + rb) * 64;
;             const float* cum = cumall + (size_t)bh * S;
;             const int jhi = 4 * qb + 3;
;             fox_cr = cum[q0]; fox_cv = cum[64 * (lane <= jhi ? lane : jhi) + 63]; fox_cq = cum[q0 + 32 * wid + r32];
;             if (!(dbg & 1)) { FOX_ISSUE(0); FOX_ISSUE(1); FOX_ISSUE(2); }
;             const bf16_t* Q = proj + ((size_t)(0 + h) * NTOK + rb + q0 + 32 * wid + r32) * 64;
; #pragma unroll
;             for (int d0 = 0; d0 < 4; ++d0) qr[d0] = *(const bf16x8*)(Q + d0 * 16 + hi * 8);
; __device__ __forceinline__ void op_mfma(const Args& a, LAS unsigned char* lds, int layer, bf16_t* outp = nullptr) {
;     pg8::DenseOrder So; So.init(a.ws + WS_ACT, a.ws + WS_WOUT + (size_t)layer * D * D * 2, NTOK, D, D, gridDim.x, blockIdx.x, (size_t)256 * 128);
;     bf16_t* xb = (bf16_t*)(a.ws + WS_XB);
;     EpiOut E{layer == 0 ? a.in[I_X] : nullptr, xb, outp ? outp : xb, (const float*)(a.ws + WS_MOD) + (size_t)layer * NB * 6144 + 2048};
;     pg8::gemm_phase<EpiOut, pg8::DenseOrder>(lds, D, So, E, 128u, (size_t)NTOK * 128);
	v_writelane_b32 v255, s4, 60
	s_or_b32 s66, s7, 2
	s_nop 0
	v_writelane_b32 v255, s5, 61
	s_lshl_b64 s[4:5], s[66:67], 13
	s_add_u32 s20, s11, s4
	s_addc_u32 s21, s12, s5
	s_add_u32 s4, s9, s4
	s_addc_u32 s5, s10, s5
	v_writelane_b32 v253, s4, 0
	s_lshl_b32 s66, s66, 6
	v_writelane_b32 v255, s20, 62
	v_writelane_b32 v253, s5, 1
	s_lshl_b64 s[4:5], s[66:67], 2
	s_add_u32 s4, s18, s4
	s_addc_u32 s5, s19, s5
	v_writelane_b32 v253, s4, 2
	s_or_b32 s66, s7, 1
	v_writelane_b32 v255, s21, 63
	v_writelane_b32 v253, s5, 3
	s_lshl_b64 s[4:5], s[66:67], 13
	s_add_u32 s20, s11, s4
	s_addc_u32 s21, s12, s5
	v_writelane_b32 v253, s20, 4
	s_add_u32 s4, s9, s4
	s_addc_u32 s5, s10, s5
	v_writelane_b32 v253, s21, 5
	v_writelane_b32 v253, s4, 6
	s_lshl_b32 s66, s66, 6
	s_mov_b32 s9, s67
	v_writelane_b32 v253, s5, 7
	s_lshl_b64 s[4:5], s[66:67], 2
	s_add_u32 s4, s18, s4
	v_writelane_b32 v253, s18, 8
	s_addc_u32 s5, s19, s5
	s_nop 0
	v_writelane_b32 v253, s19, 9
	v_writelane_b32 v253, s4, 10
	s_nop 1
	v_writelane_b32 v253, s5, 11
	s_lshl_b32 s4, s8, 15
	s_or_b32 s4, s6, s4
	s_mov_b32 s6, s16
	v_writelane_b32 v253, s6, 12
	s_add_i32 s4, s4, s16
	s_mov_b32 s8, s77
	v_writelane_b32 v253, s7, 13
	s_mov_b32 s6, s61
	s_mov_b32 s7, s67
	v_writelane_b32 v253, s4, 14
	s_lshl_b64 s[4:5], s[6:7], 9
	s_lshl_b64 s[70:71], s[8:9], 9
	v_writelane_b32 v253, s4, 15
	s_nop 1
	v_writelane_b32 v253, s5, 16
	s_add_u32 s4, s92, 0x8c00000
	s_addc_u32 s5, s93, 0
	v_writelane_b32 v253, s4, 17
	s_nop 1
	v_writelane_b32 v253, s5, 18
	s_add_u32 s4, s92, 0x1700000
	v_writelane_b32 v253, s4, 19
	s_addc_u32 s4, s93, 0
	v_writelane_b32 v253, s4, 20
	s_add_u32 s4, s92, 0x10000
	v_writelane_b32 v253, s4, 21
	s_addc_u32 s4, s93, 0
	v_writelane_b32 v253, s4, 22
	s_add_u32 s4, s92, 0x300000
	s_addc_u32 s5, s93, 0
	v_writelane_b32 v253, s4, 23
	s_nop 1
	v_writelane_b32 v253, s5, 24
	s_add_u32 s4, s92, 0x500000
	s_addc_u32 s5, s93, 0
	v_writelane_b32 v253, s4, 25
	s_cmpk_lt_i32 s61, 0x100
	s_nop 0
	v_writelane_b32 v253, s5, 26
	s_cselect_b64 s[4:5], -1, 0
	v_writelane_b32 v253, s4, 27
	s_nop 1
	v_writelane_b32 v253, s5, 28
	s_add_u32 s4, s92, 0x14400000
	s_addc_u32 s5, s93, 0
	v_writelane_b32 v253, s4, 29
	s_nop 1
	v_writelane_b32 v253, s5, 30
	s_add_i32 s4, s77, s61
	v_writelane_b32 v253, s4, 31
	s_add_u32 s4, s92, 0x7c00080
	s_addc_u32 s5, s93, 0
	s_add_i32 s2, s3, s2
	s_ashr_i32 s3, s2, 31
	s_lshr_b32 s3, s3, 27
	v_writelane_b32 v253, s4, 32
	s_add_i32 s3, s2, s3
	s_nop 0
	v_writelane_b32 v253, s5, 33
	s_and_b32 s4, s3, 0xffe0
	s_sub_i32 s2, s2, s4
	s_bfe_i32 s4, s2, 0x80000
	s_bfe_u32 s4, s4, 0x3000c
	s_add_i32 s4, s2, s4
	s_and_b32 s5, s4, 0xf8
	s_sub_i32 s2, s2, s5
	s_ashr_i32 s3, s3, 5
	s_bfe_i32 s4, s4, 0x80000
	s_lshl_b32 s3, s3, 3
	s_sext_i32_i16 s4, s4
	s_sext_i32_i8 s2, s2
	s_add_i32 s10, s3, s2
	s_ashr_i32 s2, s4, 3
	v_writelane_b32 v253, s2, 34
	s_lshr_b32 s2, s4, 3
	s_mov_b32 s4, s10
	s_ashr_i32 s11, s10, 31
	v_writelane_b32 v253, s4, 35
	s_nop 1
	v_writelane_b32 v253, s5, 36
	s_lshl_b64 s[4:5], s[10:11], 15
	s_add_u32 s4, s80, s4
	s_addc_u32 s5, s81, s5
	v_writelane_b32 v253, s14, 37
	s_bfe_i64 s[2:3], s[2:3], 0x100000
	s_lshl_b64 s[2:3], s[2:3], 19
	v_writelane_b32 v253, s15, 38
	v_writelane_b32 v253, s2, 39
	s_nop 1
	v_writelane_b32 v253, s3, 40
	s_add_u32 s2, s4, 0x4000
	s_addc_u32 s3, s5, 0
	v_writelane_b32 v253, s2, 41
	s_nop 1
	v_writelane_b32 v253, s3, 42
	s_add_u32 s2, s4, 0x400000
	v_writelane_b32 v253, s4, 43
	s_addc_u32 s3, s5, 0
	s_lshl_b64 s[52:53], s[8:9], 10
	v_writelane_b32 v253, s5, 44
	v_writelane_b32 v253, s2, 45
	s_add_i32 s64, 0, 0x13000
	s_nop 0
	v_writelane_b32 v253, s3, 46
	s_lshl_b32 s2, s61, 7
	v_writelane_b32 v253, s2, 47
	s_lshl_b32 s2, s77, 7
	v_writelane_b32 v253, s2, 48
	s_mul_i32 s2, s77, 0x3000
	v_writelane_b32 v253, s2, 49
	s_add_i32 s2, 0, 0x21c20
	v_writelane_b32 v253, s2, 50
	s_add_i32 s2, 0, 0x21c24
	v_writelane_b32 v253, s2, 51
	s_add_i32 s2, 0, 0x21000
	v_writelane_b32 v253, s2, 52
	s_add_i32 s2, 0, 0x21100
	v_writelane_b32 v253, s2, 53
	s_add_i32 s2, 0, 0x21200
	v_writelane_b32 v253, s2, 54
	s_add_i32 s2, 0, 0x21504
	v_writelane_b32 v253, s2, 55
	s_add_i32 s2, 0, 0x15040
	v_writelane_b32 v253, s2, 56
	s_add_i32 s2, 0, 0x15000
	v_writelane_b32 v253, s2, 57
	s_add_i32 s2, 0, 0x21e80
	v_writelane_b32 v253, s2, 58
	s_add_i32 s2, 0, 0x21e10
	v_writelane_b32 v253, s2, 59
	s_add_i32 s2, 0, 0x21e20
	v_writelane_b32 v253, s2, 60
	s_add_i32 s2, 0, 0x21e30
	v_writelane_b32 v253, s2, 61
	v_writelane_b32 v253, s54, 62
	s_load_dwordx2 s[4:5], s[54:55], 0x0
	s_mov_b32 s3, 0x42b17218
	v_writelane_b32 v253, s55, 63
	s_waitcnt lgkmcnt(0)
	v_writelane_b32 v254, s4, 0
	s_nop 1
	v_writelane_b32 v254, s5, 1
	s_lshl_b64 s[4:5], s[8:9], 13
	v_writelane_b32 v254, s4, 2
	s_nop 1
	v_writelane_b32 v254, s5, 3
	v_writelane_b32 v254, s6, 4
	s_lshl_b64 s[4:5], s[6:7], 12
	s_nop 0
	v_writelane_b32 v254, s7, 5
	v_writelane_b32 v254, s4, 6
	s_nop 1
	v_writelane_b32 v254, s5, 7
	s_lshl_b64 s[4:5], s[8:9], 14
	v_writelane_b32 v254, s4, 8
	s_nop 1
	v_writelane_b32 v254, s5, 9
	v_writelane_b32 v254, s8, 10
	s_lshl_b64 s[4:5], s[8:9], 12
	s_nop 0
	v_writelane_b32 v254, s9, 11
	v_writelane_b32 v254, s4, 12
	s_nop 1
	v_writelane_b32 v254, s5, 13
	v_writelane_b32 v254, s82, 14
	s_nop 1
	v_writelane_b32 v254, s83, 15
	s_branch .LBB0_104
